# rowsum via VALU adds instead of 4 ones-MFMA per tile, diff+band attention
# baseline (speedup 1.0000x reference)
; #define MFMA32(a, b, c) __builtin_amdgcn_mfma_f32_32x32x16_bf16((a), (b), (c), 0, 0, 0)
; template <int OFF> DI s16x4 at_tr_read(int vb) { s16x4 r; asm volatile("ds_read_b64_tr_b16 %0, %1 offset:%2" : "=&v"(r) : "v"(vb), "i"(OFF) : "memory"); return r; }
; DI unsigned at_cvtpk(float lo, float hi) { unsigned r; asm volatile("v_cvt_pk_bf16_f32 %0, %1, %2" : "=v"(r) : "v"(lo), "v"(hi)); return r; }
; DI float at_softmax(f32x16& p0, f32x16& p1, float& m_run, bool first, bool nearb, LAS const float* tabp, int lane) {
;     ...
; #pragma unroll
;     for (int i = 0; i < 16; ++i) p0[i] = __builtin_amdgcn_exp2f(p0[i]);
; #pragma unroll
;     for (int i = 0; i < 16; ++i) p1[i] = __builtin_amdgcn_exp2f(p1[i]);
;     return alpha;
; }
; DI bf16x8 at_pack(const f32x16& p, int s8) {
;     u32x4 w; w.x = at_cvtpk(p[s8], p[s8 + 1]); w.y = at_cvtpk(p[s8 + 2], p[s8 + 3]); w.z = at_cvtpk(p[s8 + 4], p[s8 + 5]); w.w = at_cvtpk(p[s8 + 6], p[s8 + 7]);
;     return __builtin_bit_cast(bf16x8, w);
; }
; template <int D0> DI void at_pv_block(f32x16 (&o)[4], int vb, const bf16x8 (&pf)[4]) {
;     const s16x4 l0 = at_tr_read<D0 * 512 + 0 * 4096>(vb), h0 = at_tr_read<D0 * 512 + 0 * 4096 + 2048>(vb), l1 = at_tr_read<D0 * 512 + 1 * 4096>(vb), h1 = at_tr_read<D0 * 512 + 1 * 4096 + 2048>(vb);
;     const s16x4 l2 = at_tr_read<D0 * 512 + 2 * 4096>(vb), h2 = at_tr_read<D0 * 512 + 2 * 4096 + 2048>(vb), l3 = at_tr_read<D0 * 512 + 3 * 4096>(vb), h3 = at_tr_read<D0 * 512 + 3 * 4096 + 2048>(vb);
;     asm volatile("s_waitcnt lgkmcnt(0)" ::: "memory"); __builtin_amdgcn_sched_barrier(0);
;     ...
;     o[D0] = MFMA32(AT_PK(l0, h0), pf[0], o[D0]); o[D0] = MFMA32(AT_PK(l1, h1), pf[1], o[D0]); o[D0] = MFMA32(AT_PK(l2, h2), pf[2], o[D0]); o[D0] = MFMA32(AT_PK(l3, h3), pf[3], o[D0]);
; DI void attn_unit_band(const Ctx& C, int l, int b, int h, int qt) {
;     ...
;             bf16x8 pf[4];
;             pf[0] = at_pack(p0, 0); pf[1] = at_pack(p0, 8); pf[2] = at_pack(p1, 0); pf[3] = at_pack(p1, 8);
;             ol = MFMA32(ones, pf[0], ol); ol = MFMA32(ones, pf[1], ol); ol = MFMA32(ones, pf[2], ol); ol = MFMA32(ones, pf[3], ol);
;             at_pv_block<0>(o, vb, pf); at_pv_block<1>(o, vb, pf); at_pv_block<2>(o, vb, pf); at_pv_block<3>(o, vb, pf);
.LBB0_889:
	v_exp_f32_e32 v112, v112
	v_exp_f32_e32 v113, v113
	v_exp_f32_e32 v114, v114
	v_exp_f32_e32 v115, v115
	s_mov_b32 s58, s56
	s_mov_b32 s59, s56
	v_exp_f32_e32 v152, v100
	v_exp_f32_e32 v176, v108
	v_exp_f32_e32 v177, v109
	v_subrev_u32_e32 v100, s57, v167
	v_cvt_pk_bf16_f32 v108, v112, v113
	v_cvt_pk_bf16_f32 v109, v114, v115
	s_mov_b32 s57, s56
	v_exp_f32_e32 v116, v116
	v_exp_f32_e32 v117, v117
	v_exp_f32_e32 v118, v118
	v_exp_f32_e32 v119, v119
	v_exp_f32_e32 v178, v110
	v_exp_f32_e32 v179, v111
	v_cvt_pk_bf16_f32 v110, v116, v117
	v_cvt_pk_bf16_f32 v111, v118, v119
	v_add_f32_e32 v81, v112, v113
	v_add_f32_e32 v82, v114, v115
	v_add_f32_e32 v83, v116, v117
	v_add_f32_e32 v84, v118, v119
	v_add_f32_e32 v81, v81, v82
	v_add_f32_e32 v83, v83, v84
	v_add_f32_e32 v81, v81, v83
	v_exp_f32_e32 v120, v120
	v_exp_f32_e32 v121, v121
	v_exp_f32_e32 v122, v122
	v_exp_f32_e32 v123, v123
	v_exp_f32_e32 v124, v124
	v_exp_f32_e32 v125, v125
	v_exp_f32_e32 v126, v126
	v_exp_f32_e32 v127, v127
	v_exp_f32_e32 v172, v104
	v_exp_f32_e32 v173, v105
	v_exp_f32_e32 v174, v106
	v_exp_f32_e32 v175, v107
	v_cvt_pk_bf16_f32 v104, v120, v121
	v_cvt_pk_bf16_f32 v105, v122, v123
	v_cvt_pk_bf16_f32 v106, v124, v125
	v_cvt_pk_bf16_f32 v107, v126, v127
	v_add_f32_e32 v82, v120, v121
	v_add_f32_e32 v83, v122, v123
	v_add_f32_e32 v84, v124, v125
	v_add_f32_e32 v85, v126, v127
	v_add_f32_e32 v82, v82, v83
	v_add_f32_e32 v84, v84, v85
	v_add_f32_e32 v82, v82, v84
	v_add_f32_e32 v81, v81, v82
	v_exp_f32_e32 v103, v103
	v_exp_f32_e32 v96, v96
	v_exp_f32_e32 v97, v97
	v_exp_f32_e32 v98, v98
	v_exp_f32_e32 v99, v99
	v_exp_f32_e32 v170, v101
	v_exp_f32_e32 v171, v102
	v_add_u32_e32 v180, s75, v100
	v_add_f32_e32 v82, v96, v97
	v_add_f32_e32 v83, v98, v99
	v_add_f32_e32 v84, v152, v170
	v_add_f32_e32 v85, v171, v103
	v_add_f32_e32 v86, v172, v173
	v_add_f32_e32 v87, v174, v175
	v_add_f32_e32 v88, v176, v177
	v_add_f32_e32 v89, v178, v179
	v_add_f32_e32 v82, v82, v83
	v_add_f32_e32 v84, v84, v85
	v_add_f32_e32 v86, v86, v87
	v_add_f32_e32 v88, v88, v89
	v_add_f32_e32 v82, v82, v84
	v_add_f32_e32 v86, v86, v88
	v_add_f32_e32 v82, v82, v86
	v_add_f32_e32 v81, v81, v82
	v_add_f32_e32 v80, v80, v81
	v_cvt_pk_bf16_f32 v100, v96, v97
	v_cvt_pk_bf16_f32 v101, v98, v99
	v_cvt_pk_bf16_f32 v102, v152, v170
	v_cvt_pk_bf16_f32 v103, v171, v103
	v_cvt_pk_bf16_f32 v96, v172, v173
	v_cvt_pk_bf16_f32 v97, v174, v175
	v_cvt_pk_bf16_f32 v98, v176, v177
	v_cvt_pk_bf16_f32 v99, v178, v179
	s_nop 0
	ds_read_b64_tr_b16 v[112:113], v180 offset:0
	ds_read_b64_tr_b16 v[114:115], v180 offset:0x800
	ds_read_b64_tr_b16 v[116:117], v180 offset:0x1000
	ds_read_b64_tr_b16 v[118:119], v180 offset:0x1800
	ds_read_b64_tr_b16 v[120:121], v180 offset:0x2000
	ds_read_b64_tr_b16 v[122:123], v180 offset:0x2800
	ds_read_b64_tr_b16 v[124:125], v180 offset:0x3000
	ds_read_b64_tr_b16 v[126:127], v180 offset:0x3800
	s_waitcnt lgkmcnt(0)
	s_nop 0
	v_mfma_f32_32x32x16_bf16 v[48:63], v[112:115], v[108:111], v[48:63]
	ds_read_b64_tr_b16 v[112:113], v180 offset:0x200
	ds_read_b64_tr_b16 v[114:115], v180 offset:0xa00
	v_mfma_f32_32x32x16_bf16 v[48:63], v[116:119], v[104:107], v[48:63]
	ds_read_b64_tr_b16 v[116:117], v180 offset:0x1200
	ds_read_b64_tr_b16 v[118:119], v180 offset:0x1a00
	v_mfma_f32_32x32x16_bf16 v[48:63], v[120:123], v[100:103], v[48:63]
	ds_read_b64_tr_b16 v[120:121], v180 offset:0x2200
	ds_read_b64_tr_b16 v[122:123], v180 offset:0x2a00
	v_mfma_f32_32x32x16_bf16 v[48:63], v[124:127], v[96:99], v[48:63]
	ds_read_b64_tr_b16 v[124:125], v180 offset:0x3200
	ds_read_b64_tr_b16 v[126:127], v180 offset:0x3a00
	s_waitcnt lgkmcnt(0)
	v_mfma_f32_32x32x16_bf16 v[64:79], v[112:115], v[108:111], v[64:79]
	ds_read_b64_tr_b16 v[112:113], v180 offset:0x400
	ds_read_b64_tr_b16 v[114:115], v180 offset:0xc00
	v_mfma_f32_32x32x16_bf16 v[64:79], v[116:119], v[104:107], v[64:79]
	ds_read_b64_tr_b16 v[116:117], v180 offset:0x1400
	ds_read_b64_tr_b16 v[118:119], v180 offset:0x1c00
	v_mfma_f32_32x32x16_bf16 v[64:79], v[120:123], v[100:103], v[64:79]
	ds_read_b64_tr_b16 v[120:121], v180 offset:0x2400
	ds_read_b64_tr_b16 v[122:123], v180 offset:0x2c00
	v_mfma_f32_32x32x16_bf16 v[64:79], v[124:127], v[96:99], v[64:79]
	ds_read_b64_tr_b16 v[124:125], v180 offset:0x3400
	ds_read_b64_tr_b16 v[126:127], v180 offset:0x3c00
	s_waitcnt lgkmcnt(0)
	v_mfma_f32_32x32x16_bf16 v[32:47], v[112:115], v[108:111], v[32:47]
	ds_read_b64_tr_b16 v[112:113], v180 offset:0x600
	ds_read_b64_tr_b16 v[114:115], v180 offset:0xe00
	v_mfma_f32_32x32x16_bf16 v[32:47], v[116:119], v[104:107], v[32:47]
	ds_read_b64_tr_b16 v[116:117], v180 offset:0x1600
	ds_read_b64_tr_b16 v[118:119], v180 offset:0x1e00
	v_mfma_f32_32x32x16_bf16 v[32:47], v[120:123], v[100:103], v[32:47]
	ds_read_b64_tr_b16 v[120:121], v180 offset:0x2600
	ds_read_b64_tr_b16 v[122:123], v180 offset:0x2e00
	v_mfma_f32_32x32x16_bf16 v[32:47], v[124:127], v[96:99], v[32:47]
	ds_read_b64_tr_b16 v[124:125], v180 offset:0x3600
	ds_read_b64_tr_b16 v[126:127], v180 offset:0x3e00
	s_waitcnt lgkmcnt(0)
	v_mfma_f32_32x32x16_bf16 v[16:31], v[112:115], v[108:111], v[16:31]
	s_mov_b64 s[38:39], 0
	v_mfma_f32_32x32x16_bf16 v[16:31], v[116:119], v[104:107], v[16:31]
	v_mfma_f32_32x32x16_bf16 v[16:31], v[120:123], v[100:103], v[16:31]
	v_mfma_f32_32x32x16_bf16 v[16:31], v[124:127], v[96:99], v[16:31]
	s_andn2_b64 vcc, exec, s[42:43]
	s_mov_b64 s[42:43], -1
	s_cbranch_vccnz .LBB0_879

; #define LAS __attribute__((address_space(3)))
; #define LDS_WAIT() asm volatile("s_waitcnt lgkmcnt(0)" ::: "memory")
; DI unsigned pk8(float a, float b, float c, float d) { int r = __builtin_amdgcn_cvt_pk_fp8_f32(a, b, 0, false); r = __builtin_amdgcn_cvt_pk_fp8_f32(c, d, r, true); return (unsigned)r; }
; DI float clamp8(float v) { return __builtin_amdgcn_fmed3f(v, -448.f, 448.f); }
; DI unsigned at_cvtpk(float lo, float hi) { unsigned r; asm volatile("v_cvt_pk_bf16_f32 %0, %1, %2" : "=v"(r) : "v"(lo), "v"(hi)); return r; }
; DI void at_store_rows(const u32x2 (&pk)[4][4], LAS unsigned char* wst, bf16_t* out_row0  , int r32, int hi, int lane) {
; #pragma unroll
;     for (int d0 = 0; d0 < 4; ++d0)
; #pragma unroll
;         for (int gq = 0; gq < 4; ++gq) *(LAS u32x2*)(wst + r32 * 272 + (32 * d0 + 8 * gq + 4 * hi) * 2) = pk[d0][gq];
;     LDS_WAIT();
; #pragma unroll
;     for (int k = 0; k < 8; ++k) { const int idx = k * 64 + lane, row = idx >> 4, c = idx & 15;
;         const u32x4 v = *(const LAS u32x4*)(wst + row * 272 + c * 16);
;         *(u32x4*)(out_row0 + (size_t)row * D + c * 8) = v; }
; }
; DI void attn_unit_band(const Ctx& C, int l, int b, int h, int qt) {
;     ...
;     const float inv = 1.f / ol[0];
;     if (l >= L8B) { unsigned pk8v[4][4];
; #pragma unroll
;         for (int d0 = 0; d0 < 4; ++d0)
; #pragma unroll
;             for (int gq = 0; gq < 4; ++gq) pk8v[d0][gq] = pk8(clamp8(o[d0][4 * gq] * inv), clamp8(o[d0][4 * gq + 1] * inv), clamp8(o[d0][4 * gq + 2] * inv), clamp8(o[d0][4 * gq + 3] * inv));
;         at_store_rows8(pk8v, C.lds + wid * 8704, WSP(unsigned char, WS_MIX) + (rowb + q0w) * D + h * 128, r32, hi, lane);
;     } else {
;     u32x2 pk[4][4];
; #pragma unroll
;     for (int d0 = 0; d0 < 4; ++d0)
; #pragma unroll
;         for (int gq = 0; gq < 4; ++gq) { pk[d0][gq].x = at_cvtpk(o[d0][4 * gq] * inv, o[d0][4 * gq + 1] * inv); pk[d0][gq].y = at_cvtpk(o[d0][4 * gq + 2] * inv, o[d0][4 * gq + 3] * inv); }
;     at_store_rows(pk, C.lds + wid * 8704, WSP(bf16_t, WS_MIX) + (rowb + q0w) * D + h * 128, r32, hi, lane); }
.LBB0_894:
v_lshlrev_b32_e32 v81, 2, v154
v_xor_b32_e32 v81, 0x80, v81
ds_bpermute_b32 v82, v81, v80
s_waitcnt lgkmcnt(0)
v_add_f32_e32 v80, v80, v82
	v_div_scale_f32 v0, s[38:39], v80, v80, 1.0
	v_rcp_f32_e32 v2, v0
	v_div_scale_f32 v3, vcc, 1.0, v80, 1.0
	s_lshl_b32 s31, s31, 7
	v_fma_f32 v4, -v0, v2, 1.0
	v_fmac_f32_e32 v2, v4, v2
	v_mul_f32_e32 v4, v3, v2
	v_fma_f32 v5, -v0, v4, v3
	v_fmac_f32_e32 v4, v5, v2
	v_fma_f32 v0, -v0, v4, v3
	v_div_fmas_f32 v0, v0, v2, v4
	v_div_fixup_f32 v0, v0, v80, 1.0
	v_mul_f32_e32 v97, v48, v0
	v_mul_f32_e32 v94, v50, v0
	s_mov_b64 s[38:39], -1
	s_and_b64 vcc, exec, s[44:45]
	v_mul_f32_e32 v99, v49, v0
	v_mul_f32_e32 v98, v51, v0
	v_mul_f32_e32 v95, v52, v0
	v_mul_f32_e32 v96, v53, v0
	v_mul_f32_e32 v92, v54, v0
	v_mul_f32_e32 v93, v55, v0
	v_mul_f32_e32 v88, v56, v0
	v_mul_f32_e32 v89, v57, v0
	v_mul_f32_e32 v90, v58, v0
	v_mul_f32_e32 v91, v59, v0
	v_mul_f32_e32 v86, v60, v0
	v_mul_f32_e32 v87, v61, v0
	v_mul_f32_e32 v84, v62, v0
	v_mul_f32_e32 v85, v63, v0
	v_mul_f32_e32 v80, v64, v0
	v_mul_f32_e32 v81, v65, v0
	v_mul_f32_e32 v82, v66, v0
	v_mul_f32_e32 v83, v67, v0
	v_mul_f32_e32 v66, v68, v0
	v_mul_f32_e32 v67, v69, v0
	v_mul_f32_e32 v64, v70, v0
	v_mul_f32_e32 v65, v71, v0
	v_mul_f32_e32 v60, v72, v0
	v_mul_f32_e32 v61, v73, v0
	v_mul_f32_e32 v62, v74, v0
	v_mul_f32_e32 v63, v75, v0
	v_mul_f32_e32 v58, v76, v0
	v_mul_f32_e32 v59, v77, v0
	v_mul_f32_e32 v56, v78, v0
	v_mul_f32_e32 v57, v79, v0
	v_mul_f32_e32 v52, v32, v0
	v_mul_f32_e32 v53, v33, v0
	v_mul_f32_e32 v54, v34, v0
	v_mul_f32_e32 v55, v35, v0
	v_mul_f32_e32 v50, v36, v0
	v_mul_f32_e32 v51, v37, v0
	v_mul_f32_e32 v48, v38, v0
	v_mul_f32_e32 v49, v39, v0
	v_mul_f32_e32 v40, v40, v0
	v_mul_f32_e32 v41, v41, v0
	v_mul_f32_e32 v42, v42, v0
	v_mul_f32_e32 v43, v43, v0
	v_mul_f32_e32 v38, v44, v0
	v_mul_f32_e32 v39, v45, v0
	v_mul_f32_e32 v36, v46, v0
	v_mul_f32_e32 v37, v47, v0
	v_mul_f32_e32 v32, v16, v0
	v_mul_f32_e32 v33, v17, v0
	v_mul_f32_e32 v34, v18, v0
	v_mul_f32_e32 v35, v19, v0
	v_mul_f32_e32 v18, v20, v0
	v_mul_f32_e32 v19, v21, v0
	v_mul_f32_e32 v16, v22, v0
	v_mul_f32_e32 v17, v23, v0
	v_mul_f32_e32 v12, v24, v0
	v_mul_f32_e32 v13, v25, v0
	v_mul_f32_e32 v14, v26, v0
	v_mul_f32_e32 v15, v27, v0
	v_mul_f32_e32 v10, v28, v0
	v_mul_f32_e32 v11, v29, v0
	v_mul_f32_e32 v3, v30, v0
	v_mul_f32_e32 v7, v31, v0
	s_cbranch_vccz .LBB0_896
	s_add_u32 s38, s40, s28
	s_addc_u32 s39, s41, 0
	s_lshl_b64 s[38:39], s[38:39], 12
	s_add_u32 s35, s15, s38
	v_mul_u32_u24_e32 v0, 0x110, v155
	v_cvt_pk_bf16_f32 v4, v97, v99
	v_cvt_pk_bf16_f32 v5, v94, v98
	v_cvt_pk_bf16_f32 v8, v95, v96
	v_cvt_pk_bf16_f32 v9, v92, v93
	s_addc_u32 s39, s16, s39
	s_lshl_b32 s38, s31, 1
	v_add3_u32 v0, s79, v0, v150
	v_cvt_pk_bf16_f32 v20, v88, v89
	v_cvt_pk_bf16_f32 v21, v90, v91
	v_cvt_pk_bf16_f32 v22, v86, v87
	v_cvt_pk_bf16_f32 v23, v84, v85
	v_cvt_pk_bf16_f32 v24, v80, v81
	v_cvt_pk_bf16_f32 v25, v82, v83
	v_cvt_pk_bf16_f32 v26, v66, v67
	v_cvt_pk_bf16_f32 v27, v64, v65
	v_cvt_pk_bf16_f32 v28, v60, v61
	v_cvt_pk_bf16_f32 v29, v62, v63
	v_cvt_pk_bf16_f32 v30, v58, v59
	v_cvt_pk_bf16_f32 v31, v56, v57
	v_cvt_pk_bf16_f32 v44, v52, v53
	v_cvt_pk_bf16_f32 v45, v54, v55
	v_cvt_pk_bf16_f32 v46, v50, v51
	v_cvt_pk_bf16_f32 v47, v48, v49
	v_cvt_pk_bf16_f32 v68, v40, v41
	v_cvt_pk_bf16_f32 v69, v42, v43
	v_cvt_pk_bf16_f32 v70, v38, v39
	v_cvt_pk_bf16_f32 v71, v36, v37
	v_cvt_pk_bf16_f32 v72, v32, v33
	v_cvt_pk_bf16_f32 v73, v34, v35
	v_cvt_pk_bf16_f32 v74, v18, v19
	v_cvt_pk_bf16_f32 v75, v16, v17
	v_cvt_pk_bf16_f32 v76, v12, v13
	v_cvt_pk_bf16_f32 v77, v14, v15
	v_cvt_pk_bf16_f32 v78, v10, v11
	v_cvt_pk_bf16_f32 v79, v3, v7
	s_add_u32 s38, s35, s38
	ds_write2_b64 v0, v[4:5], v[8:9] offset1:2
	ds_write2_b64 v0, v[20:21], v[22:23] offset0:4 offset1:6
	ds_write2_b64 v0, v[24:25], v[26:27] offset0:8 offset1:10
	ds_write2_b64 v0, v[28:29], v[30:31] offset0:12 offset1:14
	ds_write2_b64 v0, v[44:45], v[46:47] offset0:16 offset1:18
	ds_write2_b64 v0, v[68:69], v[70:71] offset0:20 offset1:22
	ds_write2_b64 v0, v[72:73], v[74:75] offset0:24 offset1:26
	ds_write2_b64 v0, v[76:77], v[78:79] offset0:28 offset1:30
	v_and_b32_e32 v0, 0xf0, v151
	s_addc_u32 s39, s39, 0
	v_add_u32_e32 v2, s79, v0
	s_movk_i32 s35, 0x110
	s_waitcnt lgkmcnt(0)
	v_lshl_add_u64 v[4:5], s[38:39], 0, v[0:1]
	v_mad_u64_u32 v[8:9], s[38:39], v148, s35, v[2:3]
	v_add_u32_e32 v0, 64, v154
	ds_read_b128 v[20:23], v8
	v_ashrrev_i32_e32 v28, 4, v0
	v_mad_u64_u32 v[24:25], s[38:39], v28, s35, v[2:3]
	v_ashrrev_i32_e32 v149, 31, v148
	ds_read_b128 v[24:27], v24
	v_lshlrev_b64 v[8:9], 12, v[148:149]
	v_lshl_add_u64 v[8:9], v[4:5], 0, v[8:9]
	v_ashrrev_i32_e32 v29, 31, v28
	s_waitcnt lgkmcnt(0)
	global_store_dwordx4 v[8:9], v[20:23], off
	v_lshlrev_b64 v[8:9], 12, v[28:29]
	v_lshl_add_u64 v[8:9], v[4:5], 0, v[8:9]
	v_add_u32_e32 v0, 0x80, v154
	global_store_dwordx4 v[8:9], v[24:27], off
	v_ashrrev_i32_e32 v8, 4, v0
	v_mad_u64_u32 v[20:21], s[38:39], v8, s35, v[2:3]
	v_add_u32_e32 v0, 0xc0, v154
	ds_read_b128 v[20:23], v20
	v_ashrrev_i32_e32 v28, 4, v0
	v_mad_u64_u32 v[24:25], s[38:39], v28, s35, v[2:3]
	v_ashrrev_i32_e32 v9, 31, v8
	ds_read_b128 v[24:27], v24
	v_lshlrev_b64 v[8:9], 12, v[8:9]
	v_lshl_add_u64 v[8:9], v[4:5], 0, v[8:9]
	v_ashrrev_i32_e32 v29, 31, v28
	s_waitcnt lgkmcnt(0)
	global_store_dwordx4 v[8:9], v[20:23], off
	v_lshlrev_b64 v[8:9], 12, v[28:29]
	v_add_u32_e32 v0, 0x100, v154
	v_lshl_add_u64 v[8:9], v[4:5], 0, v[8:9]
	v_ashrrev_i32_e32 v6, 4, v0
	global_store_dwordx4 v[8:9], v[24:27], off
	v_mad_u64_u32 v[8:9], s[38:39], v6, s35, v[2:3]
	s_mov_b64 s[38:39], 0
